# v35 + DSA attention: counted lgkmcnt waits for the 8-read QK fragment burst instead of a blanket lgkmcnt(0)
# baseline (speedup 1.0000x reference)
; #define LAS __attribute__((address_space(3)))
; template <int DQK, int DV, int MODE, int S> ...
;     ...
;             if (MODE == 2) {
;                 const unsigned nw = ~*(const LAS unsigned*)(lds + L::MASKOFF + (wave * S + st) * 256 + lane * 4);
; #pragma unroll
;                 for (int r = 0; r < 16; ++r) { p0[r] = __uint_as_float((unsigned)__builtin_amdgcn_sbfe((int)nw, r, 1) & 0xff800000u); p1[r] = __uint_as_float((unsigned)__builtin_amdgcn_sbfe((int)nw, 16 + r, 1) & 0xff800000u); }
;             } else if (MODE == 1) {
;                 const int n = kt >> 2; const float cv = (n == jblk || ((selb >> n) & 1u)) ? 0.f : -INFINITY;
; #pragma unroll
;                 for (int r = 0; r < 16; ++r) { p0[r] = cv; p1[r] = cv; }
;             } else {
; #pragma unroll
;                 for (int r = 0; r < 16; ++r) { p0[r] = 0.f; p1[r] = 0.f; }
;             }
; #pragma unroll
;             for (int db = 0; db < DQK / 64; ++db) {
;                 f16x8 kf0[4], kf1[4];
; #pragma unroll
;                 for (int d = 0; d < 4; ++d) { kf0[d] = *(const LAS f16x8*)(sb + koff[4 * db + d]); kf1[d] = *(const LAS f16x8*)(sb + koff[4 * db + d] + 32 * L::CPRK * 16); }
;                 __builtin_amdgcn_sched_barrier(0);
; #pragma unroll
;                 for (int d = 0; d < 4; ++d) {
;                     p0 = __builtin_amdgcn_mfma_f32_32x32x16_f16(kf0[d], qf[4 * db + d], p0, 0, 0, 0);
;                     p1 = __builtin_amdgcn_mfma_f32_32x32x16_f16(kf1[d], qf[4 * db + d], p1, 0, 0, 0); }
;                 __builtin_amdgcn_sched_barrier(0);
;             }
;             f16x8 vfa[NB_], vfb[NB_];
;             FA_VREADD(vfa, 0);
.LBB0_1042:
	s_cmp_gt_u32 s42, s40
	s_cbranch_scc1 .LBB0_1035
	v_lshl_add_u32 v0, v146, 2, s4
	v_lshl_add_u32 v0, s44, 8, v0
	ds_read_b32 v0, v0
	s_lshl_b32 s36, s44, 14
	v_add3_u32 v82, s36, v157, v156
	ds_read_b128 v[130:133], v82
	ds_read_b128 v[134:137], v82 offset:8192
	v_add3_u32 v82, s36, v158, v156
	s_waitcnt lgkmcnt(0)
	v_and_b32_e32 v66, 0x20000, v0
	v_and_b32_e32 v68, 0x10000, v0
	v_cmp_eq_u32_e32 vcc, 0, v66
	v_and_b32_e32 v70, 0x40000, v0
	v_and_b32_e32 v72, 0x100000, v0
	v_cndmask_b32_e32 v67, 0, v233, vcc
	v_cmp_eq_u32_e32 vcc, 0, v68
	v_and_b32_e32 v68, 0x80000, v0
	v_and_b32_e32 v74, 0x400000, v0
	v_cndmask_b32_e32 v66, 0, v233, vcc
	v_cmp_eq_u32_e32 vcc, 0, v68
	v_and_b32_e32 v76, 0x1000000, v0
	v_and_b32_e32 v78, 0x4000000, v0
	v_cndmask_b32_e32 v69, 0, v233, vcc
	v_cmp_eq_u32_e32 vcc, 0, v70
	v_and_b32_e32 v70, 0x200000, v0
	v_and_b32_e32 v80, 0x10000000, v0
	v_cndmask_b32_e32 v68, 0, v233, vcc
	v_cmp_eq_u32_e32 vcc, 0, v70
	v_and_b32_e32 v81, 0x8000, v0
	ds_read_b128 v[138:141], v82
	ds_read_b128 v[142:145], v82 offset:8192
	v_cndmask_b32_e32 v71, 0, v233, vcc
	v_cmp_eq_u32_e32 vcc, 0, v72
	v_and_b32_e32 v72, 0x800000, v0
	v_add3_u32 v82, s36, v159, v156
	v_cndmask_b32_e32 v70, 0, v233, vcc
	v_cmp_eq_u32_e32 vcc, 0, v72
	ds_read_b128 v[180:183], v82
	ds_read_b128 v[184:187], v82 offset:8192
	v_cndmask_b32_e32 v73, 0, v233, vcc
	v_cmp_eq_u32_e32 vcc, 0, v74
	v_and_b32_e32 v74, 0x2000000, v0
	v_add3_u32 v82, s36, v160, v156
	v_cndmask_b32_e32 v72, 0, v233, vcc
	v_cmp_eq_u32_e32 vcc, 0, v74
	ds_read_b128 v[188:191], v82
	ds_read_b128 v[192:195], v82 offset:8192
	v_cndmask_b32_e32 v75, 0, v233, vcc
	v_cmp_eq_u32_e32 vcc, 0, v76
	v_and_b32_e32 v76, 0x8000000, v0
	s_nop 0
	v_cndmask_b32_e32 v74, 0, v233, vcc
	v_cmp_eq_u32_e32 vcc, 0, v76
	s_nop 1
	v_cndmask_b32_e32 v77, 0, v233, vcc
	v_cmp_eq_u32_e32 vcc, 0, v78
	v_and_b32_e32 v78, 0x20000000, v0
	s_nop 0
	v_cndmask_b32_e32 v76, 0, v233, vcc
	v_cmp_eq_u32_e32 vcc, 0, v78
	s_nop 1
	v_cndmask_b32_e32 v79, 0, v233, vcc
	v_cmp_eq_u32_e32 vcc, 0, v80
	v_and_b32_e32 v80, 2.0, v0
	s_nop 0
	v_cndmask_b32_e32 v78, 0, v233, vcc
	v_cmp_eq_u32_e32 vcc, 0, v80
	s_nop 1
	v_cndmask_b32_e32 v80, 0, v233, vcc
	v_cmp_ne_u32_e32 vcc, 0, v81
	v_and_b32_e32 v81, 0x4000, v0
	s_nop 0
	v_cndmask_b32_e64 v97, v233, 0, vcc
	v_cmp_ne_u32_e32 vcc, 0, v81
	v_and_b32_e32 v81, 0x2000, v0
	s_nop 0
	v_cndmask_b32_e64 v96, v233, 0, vcc
	v_cmp_ne_u32_e32 vcc, 0, v81
	v_and_b32_e32 v81, 0x1000, v0
	s_nop 0
	v_cndmask_b32_e64 v95, v233, 0, vcc
	v_cmp_ne_u32_e32 vcc, 0, v81
	v_and_b32_e32 v81, 0x800, v0
	s_nop 0
	v_cndmask_b32_e64 v94, v233, 0, vcc
	v_cmp_ne_u32_e32 vcc, 0, v81
	v_and_b32_e32 v81, 0x400, v0
	s_nop 0
	v_cndmask_b32_e64 v93, v233, 0, vcc
	v_cmp_ne_u32_e32 vcc, 0, v81
	v_and_b32_e32 v81, 0x200, v0
	s_nop 0
	v_cndmask_b32_e64 v92, v233, 0, vcc
	v_cmp_ne_u32_e32 vcc, 0, v81
	v_and_b32_e32 v81, 0x100, v0
	s_nop 0
	v_cndmask_b32_e64 v91, v233, 0, vcc
	v_cmp_ne_u32_e32 vcc, 0, v81
	v_and_b32_e32 v81, 0x80, v0
	s_nop 0
	v_cndmask_b32_e64 v90, v233, 0, vcc
	v_cmp_ne_u32_e32 vcc, 0, v81
	v_and_b32_e32 v81, 64, v0
	s_nop 0
	v_cndmask_b32_e64 v89, v233, 0, vcc
	v_cmp_ne_u32_e32 vcc, 0, v81
	v_and_b32_e32 v81, 32, v0
	s_nop 0
	v_cndmask_b32_e64 v88, v233, 0, vcc
	v_cmp_ne_u32_e32 vcc, 0, v81
	v_and_b32_e32 v81, 16, v0
	s_nop 0
	v_cndmask_b32_e64 v87, v233, 0, vcc
	v_cmp_ne_u32_e32 vcc, 0, v81
	v_and_b32_e32 v81, 8, v0
	s_nop 0
	v_cndmask_b32_e64 v86, v233, 0, vcc
	v_cmp_ne_u32_e32 vcc, 0, v81
	v_and_b32_e32 v81, 4, v0
	s_nop 0
	v_cndmask_b32_e64 v85, v233, 0, vcc
	v_cmp_ne_u32_e32 vcc, 0, v81
	v_and_b32_e32 v81, 2, v0
	s_nop 0
	v_cndmask_b32_e64 v84, v233, 0, vcc
	v_cmp_ne_u32_e32 vcc, 0, v81
	v_and_b32_e32 v81, 1, v0
	s_nop 0
	v_cndmask_b32_e64 v83, v233, 0, vcc
	v_cmp_eq_u32_e32 vcc, 1, v81
	s_nop 1
	v_cndmask_b32_e64 v82, v233, 0, vcc
	v_cmp_gt_i32_e32 vcc, 0, v0
	s_nop 1
	v_cndmask_b32_e64 v81, v233, 0, vcc
	v_mfma_f32_32x32x16_f16 v[82:97], v[130:133], v[122:125], v[82:97]
	s_nop 0
	v_mfma_f32_32x32x16_f16 v[66:81], v[134:137], v[122:125], v[66:81]
	s_waitcnt lgkmcnt(0)
	v_mfma_f32_32x32x16_f16 v[82:97], v[138:141], v[98:101], v[82:97]
	v_mfma_f32_32x32x16_f16 v[66:81], v[142:145], v[98:101], v[66:81]
	v_mfma_f32_32x32x16_f16 v[82:97], v[180:183], v[102:105], v[82:97]
	v_mfma_f32_32x32x16_f16 v[66:81], v[184:187], v[102:105], v[66:81]
	v_mfma_f32_32x32x16_f16 v[82:97], v[188:191], v[106:109], v[82:97]
	v_mfma_f32_32x32x16_f16 v[66:81], v[192:195], v[106:109], v[66:81]
	v_add3_u32 v0, s36, v161, v156
	ds_read_b128 v[130:133], v0
	ds_read_b128 v[134:137], v0 offset:8192
	v_add3_u32 v0, s36, v162, v156
	ds_read_b128 v[138:141], v0
	ds_read_b128 v[142:145], v0 offset:8192
	v_add3_u32 v0, s36, v163, v156
	ds_read_b128 v[180:183], v0
	ds_read_b128 v[184:187], v0 offset:8192
	v_add3_u32 v0, s36, v164, v156
	ds_read_b128 v[188:191], v0
	ds_read_b128 v[192:195], v0 offset:8192
	s_waitcnt lgkmcnt(7)
	v_mfma_f32_32x32x16_f16 v[82:97], v[130:133], v[110:113], v[82:97]
	v_add3_u32 v130, s36, v166, v165
	v_add_u32_e32 v0, v130, v167
	v_add3_u32 v131, s36, v171, v165
	v_add_u32_e32 v179, v131, v172
	s_waitcnt lgkmcnt(6)
	v_mfma_f32_32x32x16_f16 v[66:81], v[134:137], v[110:113], v[66:81]
	s_waitcnt lgkmcnt(5)
	v_mfma_f32_32x32x16_f16 v[82:97], v[138:141], v[114:117], v[82:97]
	s_waitcnt lgkmcnt(4)
	v_mfma_f32_32x32x16_f16 v[66:81], v[142:145], v[114:117], v[66:81]
	s_waitcnt lgkmcnt(3)
	v_mfma_f32_32x32x16_f16 v[82:97], v[180:183], v[118:121], v[82:97]
	v_add_u32_e32 v182, v130, v169
	v_add_u32_e32 v180, v130, v168
	v_add_u32_e32 v181, v131, v173
	s_waitcnt vmcnt(0)
	ds_read_b64_tr_b16 v[138:139], v0
	ds_read_b64_tr_b16 v[140:141], v179
	ds_read_b64_tr_b16 v[134:135], v180
	ds_read_b64_tr_b16 v[136:137], v181
	v_add_u32_e32 v183, v131, v174
	s_waitcnt lgkmcnt(6)
	v_mfma_f32_32x32x16_f16 v[66:81], v[184:187], v[118:121], v[66:81]
	v_add_u32_e32 v184, v130, v170
	v_add_u32_e32 v185, v131, v175
	ds_read_b64_tr_b16 v[142:143], v182
	ds_read_b64_tr_b16 v[144:145], v183
	ds_read_b64_tr_b16 v[130:131], v184
	ds_read_b64_tr_b16 v[132:133], v185
	s_waitcnt lgkmcnt(9)
	v_mfma_f32_32x32x16_f16 v[82:97], v[188:191], v[126:129], v[82:97]
	s_waitcnt lgkmcnt(8)
	v_mfma_f32_32x32x16_f16 v[66:81], v[192:195], v[126:129], v[66:81]
	s_cmpk_gt_i32 s41, 0x7f
	s_cbranch_scc1 .LBB0_1045
; #define LAS __attribute__((address_space(3)))
; template <int DQK, int DV, int MODE, int S> ...
;     ...
;             if (qpos0 - (k0 + 63) < 128) {
;                 const int j0 = 224 - (qpos0 + r32 - k0 - 4 * hi), sf = j0 & 1; const LAS float* rp = tab + sf * TAB2 + (j0 - sf);
; #pragma unroll
;                 for (int g = 0; g < 4; ++g) { const f32x2 x0 = *(const LAS f32x2*)(rp + 8 * g), x1 = *(const LAS f32x2*)(rp + 8 * g + 2), y0 = *(const LAS f32x2*)(rp + 32 + 8 * g), y1 = *(const LAS f32x2*)(rp + 34 + 8 * g);
;                     p0[4 * g] += x0.x; p0[4 * g + 1] += x0.y; p0[4 * g + 2] += x1.x; p0[4 * g + 3] += x1.y; p1[4 * g] += y0.x; p1[4 * g + 1] += y0.y; p1[4 * g + 2] += y1.x; p1[4 * g + 3] += y1.y; }
;             }
	v_add_u32_e32 v186, s42, v177
	v_and_b32_e32 v186, 0x3ffffffe, v186
	v_lshl_add_u32 v224, v186, 2, v176
	ds_read2_b64 v[186:189], v224 offset0:112 offset1:113
	ds_read2_b64 v[190:193], v224 offset0:116 offset1:117
	ds_read2_b64 v[194:197], v224 offset0:120 offset1:121
	ds_read2_b64 v[208:211], v224 offset0:124 offset1:125
	ds_read2_b64 v[212:215], v224 offset0:128 offset1:129
	ds_read2_b64 v[216:219], v224 offset0:132 offset1:133
	ds_read2_b64 v[220:223], v224 offset0:136 offset1:137
	ds_read2_b64 v[224:227], v224 offset0:140 offset1:141
	s_waitcnt lgkmcnt(4)
	v_pk_add_f32 v[94:95], v[94:95], v[208:209]
	v_pk_add_f32 v[90:91], v[90:91], v[194:195]
	v_pk_add_f32 v[86:87], v[86:87], v[190:191]
	v_pk_add_f32 v[96:97], v[96:97], v[210:211]
	v_pk_add_f32 v[92:93], v[92:93], v[196:197]
	v_pk_add_f32 v[88:89], v[88:89], v[192:193]
	v_pk_add_f32 v[84:85], v[84:85], v[188:189]
	v_pk_add_f32 v[82:83], v[82:83], v[186:187]
	s_waitcnt lgkmcnt(0)
	v_pk_add_f32 v[78:79], v[78:79], v[224:225]
	v_pk_add_f32 v[74:75], v[74:75], v[220:221]
	v_pk_add_f32 v[70:71], v[70:71], v[216:217]
	v_pk_add_f32 v[80:81], v[80:81], v[226:227]
	v_pk_add_f32 v[76:77], v[76:77], v[222:223]
	v_pk_add_f32 v[72:73], v[72:73], v[218:219]
	v_pk_add_f32 v[68:69], v[68:69], v[214:215]
	v_pk_add_f32 v[66:67], v[66:67], v[212:213]
